# code placement: main instruction stream shifted by 4 bytes (one s_nop at entry)
# baseline (speedup 1.0000x reference)
_Z7na_mainPKDF16_PKhS0_PKfS4_S4_S4_Pf:
	s_nop 0
	s_lshl_b32 s3, s2, 5
	s_and_b32 s3, s3, 0xe0
	s_ashr_i32 s2, s2, 3
	s_add_i32 s3, s3, s2
	s_ashr_i32 s2, s3, 6
	s_lshl_b32 s3, s3, 5
	s_and_b32 s14, s3, 0x7e0
	v_mov_b32_e32 v1, 0x7c0
	s_load_dwordx8 s[4:11], s[0:1], 0x0
	s_load_dwordx2 s[18:19], s[0:1], 0x20
	s_load_dwordx2 s[28:29], s[0:1], 0x28
	s_load_dwordx2 s[34:35], s[0:1], 0x30
	s_load_dwordx2 s[30:31], s[0:1], 0x38
	v_med3_u32 v1, s14, 32, v1
	v_subrev_u32_e32 v97, 32, v1
	s_ashr_i32 s3, s2, 31
	v_lshlrev_b32_e32 v58, 1, v97
	s_lshl_b64 s[12:13], s[2:3], 12
	v_mov_b32_e32 v59, 0
	v_sub_u32_e32 v60, s14, v97
	v_lshl_add_u64 v[10:11], s[12:13], 0, v[58:59]
	v_lshlrev_b64 v[2:3], 9, v[10:11]
	v_lshl_or_b32 v22, v60, 6, v0
	s_waitcnt lgkmcnt(0)
	s_load_dword s32, s[28:29], 0x0
	v_and_b32_e32 v208, 31, v0
	v_lshlrev_b32_e32 v208, 5, v208
	global_load_dwordx4 v[192:195], v208, s[18:19]
	global_load_dwordx4 v[196:199], v208, s[18:19] offset:16
	v_lshl_add_u64 v[20:21], s[4:5], 0, v[2:3]
	v_ashrrev_i32_e32 v23, 31, v22
	v_lshl_add_u64 v[2:3], v[22:23], 4, v[20:21]
	global_load_dwordx4 v[12:15], v[2:3], off
	v_or_b32_e32 v28, 0x200, v22
	v_ashrrev_i32_e32 v29, 31, v28
	v_lshl_add_u64 v[2:3], v[28:29], 4, v[20:21]
	global_load_dwordx4 v[16:19], v[2:3], off
	v_or_b32_e32 v184, 0x400, v22
	v_ashrrev_i32_e32 v185, 31, v184
	v_lshl_add_u64 v[184:185], v[184:185], 4, v[20:21]
	v_or_b32_e32 v188, 0x600, v22
	v_ashrrev_i32_e32 v189, 31, v188
	v_lshl_add_u64 v[188:189], v[188:189], 4, v[20:21]
	global_load_dwordx4 v[184:187], v[184:185], off
	global_load_dwordx4 v[188:191], v[188:189], off
	v_lshrrev_b32_e32 v99, 6, v0
	v_and_b32_e32 v98, 63, v0
	v_lshlrev_b32_e32 v118, 13, v99
	v_lshl_or_b32 v58, v98, 4, v118
	v_and_b32_e32 v58, 0xfff0, v58
	v_add_u32_e32 v251, 0x1000, v58
	s_movk_i32 s15, 0x1000
	v_lshl_add_u64 v[24:25], s[6:7], 0, v[58:59]
	v_or_b32_e32 v32, 0x400, v22
	v_or_b32_e32 v62, 0x600, v22
	v_add_co_u32_e32 v64, vcc, s15, v24
	s_mov_b64 s[12:13], 0x1000
	s_mov_b64 s[16:17], 0x1800
	v_lshlrev_b32_e32 v72, 1, v60
	v_lshrrev_b32_e32 v23, 5, v22
	v_and_b32_e32 v34, 32, v22
	v_ashrrev_i32_e32 v33, 31, v32
	v_ashrrev_i32_e32 v63, 31, v62
	v_addc_co_u32_e32 v65, vcc, 0, v25, vcc
	global_load_dwordx4 v[6:9], v58, s[6:7] offset:1024
	global_load_dwordx4 v[2:5], v58, s[6:7]
	global_load_dwordx4 v[54:57], v58, s[6:7] offset:3072
	global_load_dwordx4 v[50:53], v58, s[6:7] offset:2048
	v_lshrrev_b32_e32 v58, 6, v22
	v_bfe_u32 v73, v22, 8, 2
	v_lshl_add_u64 v[26:27], v[24:25], 0, s[12:13]
	v_lshl_add_u64 v[24:25], v[24:25], 0, s[16:17]
	v_cmp_ne_u32_e32 vcc, 0, v34
	v_sub_u32_e32 v75, v23, v72
	global_load_dwordx4 v[42:45], v251, s[6:7]
	global_load_dwordx4 v[46:49], v251, s[6:7] offset:1024
	global_load_dwordx4 v[34:37], v251, s[6:7] offset:2048
	global_load_dwordx4 v[38:41], v251, s[6:7] offset:3072
	v_mov_b32_e32 v61, 0x60
	v_cndmask_b32_e32 v74, 0, v61, vcc
	v_add_u32_e32 v33, v74, v58
	v_lshlrev_b32_e32 v64, 2, v33
	v_bfe_u32 v96, v0, 4, 1
	v_and_b32_e32 v100, 15, v0
	v_mov_b32_e32 v30, v59
	v_mov_b32_e32 v31, v59
	v_and_b32_e32 v64, 12, v64
	v_mul_u32_u24_e32 v29, 0xc000, v96
	v_bitop3_b32 v64, v64, v100, v73 bitop3:0x36
	v_lshl_or_b32 v64, v64, 4, v29
	v_lshlrev_b32_e32 v63, 1, v75
	v_lshl_add_u32 v33, v33, 8, v64
	v_bfe_u32 v71, v0, 1, 4
	v_and_b32_e32 v70, 32, v0
	v_lshlrev_b32_e32 v1, 3, v0
	v_lshrrev_b32_e32 v58, 1, v75
	v_and_b32_e32 v1, 8, v1
	v_add_lshl_u32 v58, v58, v70, 8
	v_lshlrev_b32_e32 v121, 3, v99
	v_bfe_u32 v101, v0, 4, 2
	v_lshlrev_b32_e32 v102, 2, v101
	v_and_b32_e32 v116, 31, v0
	v_bfe_u32 v119, v0, 5, 1
	v_lshlrev_b32_e32 v124, 1, v119
	v_lshlrev_b32_e32 v117, 8, v116
	v_lshrrev_b32_e32 v95, 4, v0
	s_movk_i32 s16, 0x60
	s_mov_b32 s17, 0xc000
	v_and_b32_e32 v211, 3, v99
	v_lshrrev_b32_e32 v212, 2, v99
	v_lshl_or_b32 v211, v211, 2, v212
	v_xor_b32_e32 v213, v100, v211
	v_mul_u32_u24_e32 v214, 0x60, v119
	v_add3_u32 v214, v214, v60, v99
	v_mul_u32_u24_e32 v215, 0xc000, v96
	v_lshl_add_u32 v214, v214, 8, v215
	v_lshl_or_b32 v220, v213, 4, v214
	v_xor_b32_e32 v221, 32, v220
	v_xor_b32_e32 v216, v71, v211
	v_lshl_add_u32 v217, v119, 5, v99
	v_lshlrev_b32_e32 v217, 8, v217
	v_lshl_or_b32 v216, v216, 4, v217
	v_or_b32_e32 v216, v216, v1
	v_add_u32_e32 v222, 0x23800, v216
	v_xor_b32_e32 v223, 32, v222
	s_waitcnt vmcnt(11)
	ds_write_b128 v220, v[12:15]
	v_fma_mix_f32 v200, v192, v12, 0 op_sel_hi:[0,1,0]
	v_fma_mix_f32 v201, v193, v12, 0 op_sel:[0,1,0] op_sel_hi:[0,1,0]
	v_cvt_f32_f16_e32 v211, v12
	v_cvt_f32_f16_sdwa v212, v12 dst_sel:DWORD dst_unused:UNUSED_PAD src0_sel:WORD_1
	v_fma_mix_f32 v200, v194, v13, v200 op_sel_hi:[0,1,0]
	v_fma_mix_f32 v201, v195, v13, v201 op_sel:[0,1,0] op_sel_hi:[0,1,0]
	v_cvt_f32_f16_e32 v213, v13
	v_cvt_f32_f16_sdwa v214, v13 dst_sel:DWORD dst_unused:UNUSED_PAD src0_sel:WORD_1
	v_fma_mix_f32 v200, v196, v14, v200 op_sel_hi:[0,1,0]
	v_fma_mix_f32 v201, v197, v14, v201 op_sel:[0,1,0] op_sel_hi:[0,1,0]
	v_cvt_f32_f16_e32 v215, v14
	v_cvt_f32_f16_sdwa v216, v14 dst_sel:DWORD dst_unused:UNUSED_PAD src0_sel:WORD_1
	v_fma_mix_f32 v200, v198, v15, v200 op_sel_hi:[0,1,0]
	v_fma_mix_f32 v201, v199, v15, v201 op_sel:[0,1,0] op_sel_hi:[0,1,0]
	v_cvt_f32_f16_e32 v217, v15
	v_cvt_f32_f16_sdwa v218, v15 dst_sel:DWORD dst_unused:UNUSED_PAD src0_sel:WORD_1
	v_cvt_pk_fp8_f32 v224, v211, v212
	v_cvt_pk_fp8_f32 v225, v215, v216
	v_cvt_pk_fp8_f32 v224, v213, v214 op_sel:[0,0,1]
	v_cvt_pk_fp8_f32 v225, v217, v218 op_sel:[0,0,1]
	s_nop 0
	ds_write_b64 v222, v[224:225]
	s_waitcnt vmcnt(10)
	ds_write_b128 v221, v[16:19] offset:2048
	v_fma_mix_f32 v202, v192, v16, 0 op_sel_hi:[0,1,0]
	v_fma_mix_f32 v203, v193, v16, 0 op_sel:[0,1,0] op_sel_hi:[0,1,0]
	v_cvt_f32_f16_e32 v211, v16
	v_cvt_f32_f16_sdwa v212, v16 dst_sel:DWORD dst_unused:UNUSED_PAD src0_sel:WORD_1
	v_fma_mix_f32 v202, v194, v17, v202 op_sel_hi:[0,1,0]
	v_fma_mix_f32 v203, v195, v17, v203 op_sel:[0,1,0] op_sel_hi:[0,1,0]
	v_cvt_f32_f16_e32 v213, v17
	v_cvt_f32_f16_sdwa v214, v17 dst_sel:DWORD dst_unused:UNUSED_PAD src0_sel:WORD_1
	v_fma_mix_f32 v202, v196, v18, v202 op_sel_hi:[0,1,0]
	v_fma_mix_f32 v203, v197, v18, v203 op_sel:[0,1,0] op_sel_hi:[0,1,0]
	v_cvt_f32_f16_e32 v215, v18
	v_cvt_f32_f16_sdwa v216, v18 dst_sel:DWORD dst_unused:UNUSED_PAD src0_sel:WORD_1
	v_fma_mix_f32 v202, v198, v19, v202 op_sel_hi:[0,1,0]
	v_fma_mix_f32 v203, v199, v19, v203 op_sel:[0,1,0] op_sel_hi:[0,1,0]
	v_cvt_f32_f16_e32 v217, v19
	v_cvt_f32_f16_sdwa v218, v19 dst_sel:DWORD dst_unused:UNUSED_PAD src0_sel:WORD_1
	v_cvt_pk_fp8_f32 v226, v211, v212
	v_cvt_pk_fp8_f32 v227, v215, v216
	v_cvt_pk_fp8_f32 v226, v213, v214 op_sel:[0,0,1]
	v_cvt_pk_fp8_f32 v227, v217, v218 op_sel:[0,0,1]
	s_nop 0
	ds_write_b64 v223, v[226:227] offset:2048
	s_waitcnt vmcnt(9)
	ds_write_b128 v220, v[184:187] offset:4096
	v_fma_mix_f32 v204, v192, v184, 0 op_sel_hi:[0,1,0]
	v_fma_mix_f32 v205, v193, v184, 0 op_sel:[0,1,0] op_sel_hi:[0,1,0]
	v_cvt_f32_f16_e32 v211, v184
	v_cvt_f32_f16_sdwa v212, v184 dst_sel:DWORD dst_unused:UNUSED_PAD src0_sel:WORD_1
	v_fma_mix_f32 v204, v194, v185, v204 op_sel_hi:[0,1,0]
	v_fma_mix_f32 v205, v195, v185, v205 op_sel:[0,1,0] op_sel_hi:[0,1,0]
	v_cvt_f32_f16_e32 v213, v185
	v_cvt_f32_f16_sdwa v214, v185 dst_sel:DWORD dst_unused:UNUSED_PAD src0_sel:WORD_1
	v_fma_mix_f32 v204, v196, v186, v204 op_sel_hi:[0,1,0]
	v_fma_mix_f32 v205, v197, v186, v205 op_sel:[0,1,0] op_sel_hi:[0,1,0]
	v_cvt_f32_f16_e32 v215, v186
	v_cvt_f32_f16_sdwa v216, v186 dst_sel:DWORD dst_unused:UNUSED_PAD src0_sel:WORD_1
	v_fma_mix_f32 v204, v198, v187, v204 op_sel_hi:[0,1,0]
	v_fma_mix_f32 v205, v199, v187, v205 op_sel:[0,1,0] op_sel_hi:[0,1,0]
	v_cvt_f32_f16_e32 v217, v187
	v_cvt_f32_f16_sdwa v218, v187 dst_sel:DWORD dst_unused:UNUSED_PAD src0_sel:WORD_1
	v_cvt_pk_fp8_f32 v228, v211, v212
	v_cvt_pk_fp8_f32 v229, v215, v216
	v_cvt_pk_fp8_f32 v228, v213, v214 op_sel:[0,0,1]
	v_cvt_pk_fp8_f32 v229, v217, v218 op_sel:[0,0,1]
	s_nop 0
	ds_write_b64 v222, v[228:229] offset:4096
	s_waitcnt vmcnt(8)
	ds_write_b128 v221, v[188:191] offset:6144
	v_fma_mix_f32 v206, v192, v188, 0 op_sel_hi:[0,1,0]
	v_fma_mix_f32 v207, v193, v188, 0 op_sel:[0,1,0] op_sel_hi:[0,1,0]
	v_cvt_f32_f16_e32 v211, v188
	v_cvt_f32_f16_sdwa v212, v188 dst_sel:DWORD dst_unused:UNUSED_PAD src0_sel:WORD_1
	v_fma_mix_f32 v206, v194, v189, v206 op_sel_hi:[0,1,0]
	v_fma_mix_f32 v207, v195, v189, v207 op_sel:[0,1,0] op_sel_hi:[0,1,0]
	v_cvt_f32_f16_e32 v213, v189
	v_cvt_f32_f16_sdwa v214, v189 dst_sel:DWORD dst_unused:UNUSED_PAD src0_sel:WORD_1
	v_fma_mix_f32 v206, v196, v190, v206 op_sel_hi:[0,1,0]
	v_fma_mix_f32 v207, v197, v190, v207 op_sel:[0,1,0] op_sel_hi:[0,1,0]
	v_cvt_f32_f16_e32 v215, v190
	v_cvt_f32_f16_sdwa v216, v190 dst_sel:DWORD dst_unused:UNUSED_PAD src0_sel:WORD_1
	v_fma_mix_f32 v206, v198, v191, v206 op_sel_hi:[0,1,0]
	v_fma_mix_f32 v207, v199, v191, v207 op_sel:[0,1,0] op_sel_hi:[0,1,0]
	v_cvt_f32_f16_e32 v217, v191
	v_cvt_f32_f16_sdwa v218, v191 dst_sel:DWORD dst_unused:UNUSED_PAD src0_sel:WORD_1
	v_cvt_pk_fp8_f32 v230, v211, v212
	v_cvt_pk_fp8_f32 v231, v215, v216
	v_cvt_pk_fp8_f32 v230, v213, v214 op_sel:[0,0,1]
	v_cvt_pk_fp8_f32 v231, v217, v218 op_sel:[0,0,1]
	s_nop 0
	ds_write_b64 v223, v[230:231] offset:6144
	v_add_f32_e32 v200, v200, v201
	v_add_f32_e32 v202, v202, v203
	v_add_f32_e32 v204, v204, v205
	v_add_f32_e32 v206, v206, v207
	v_lshlrev_b32_e32 v208, 7, v119
	v_lshl_add_u32 v208, v99, 2, v208
	v_add_u32_e32 v208, 0x27800, v208
	v_add_f32_dpp v200, v200, v200 quad_perm:[1,0,3,2] row_mask:0xf bank_mask:0xf
	v_add_f32_dpp v202, v202, v202 quad_perm:[1,0,3,2] row_mask:0xf bank_mask:0xf
	v_add_f32_dpp v204, v204, v204 quad_perm:[1,0,3,2] row_mask:0xf bank_mask:0xf
	v_add_f32_dpp v206, v206, v206 quad_perm:[1,0,3,2] row_mask:0xf bank_mask:0xf
	v_add_f32_dpp v200, v200, v200 quad_perm:[2,3,0,1] row_mask:0xf bank_mask:0xf
	v_add_f32_dpp v202, v202, v202 quad_perm:[2,3,0,1] row_mask:0xf bank_mask:0xf
	v_add_f32_dpp v204, v204, v204 quad_perm:[2,3,0,1] row_mask:0xf bank_mask:0xf
	v_add_f32_dpp v206, v206, v206 quad_perm:[2,3,0,1] row_mask:0xf bank_mask:0xf
	v_add_f32_dpp v200, v200, v200 row_half_mirror row_mask:0xf bank_mask:0xf
	v_add_f32_dpp v202, v202, v202 row_half_mirror row_mask:0xf bank_mask:0xf
	v_add_f32_dpp v204, v204, v204 row_half_mirror row_mask:0xf bank_mask:0xf
	v_add_f32_dpp v206, v206, v206 row_half_mirror row_mask:0xf bank_mask:0xf
	v_add_f32_dpp v200, v200, v200 row_mirror row_mask:0xf bank_mask:0xf
	v_add_f32_dpp v202, v202, v202 row_mirror row_mask:0xf bank_mask:0xf
	v_add_f32_dpp v204, v204, v204 row_mirror row_mask:0xf bank_mask:0xf
	v_add_f32_dpp v206, v206, v206 row_mirror row_mask:0xf bank_mask:0xf
	v_add_f32_dpp v200, v200, v200 row_bcast:15 row_mask:0xa bank_mask:0xf
	v_add_f32_dpp v202, v202, v202 row_bcast:15 row_mask:0xa bank_mask:0xf
	v_add_f32_dpp v204, v204, v204 row_bcast:15 row_mask:0xa bank_mask:0xf
	v_add_f32_dpp v206, v206, v206 row_bcast:15 row_mask:0xa bank_mask:0xf
	s_mov_b32 exec_lo, 0xffff0000
	s_mov_b32 exec_hi, 0xffff0000
	ds_write_b32 v208, v200
	ds_write_b32 v208, v202 offset:32
	ds_write_b32 v208, v204 offset:64
	ds_write_b32 v208, v206 offset:96
	s_mov_b64 exec, -1
	v_lshlrev_b32_e32 v201, 7, v99
	v_lshl_or_b32 v201, v119, 4, v201
	global_load_dwordx4 v[184:187], v201, s[10:11]
	global_load_dwordx4 v[188:191], v201, s[10:11] offset:32
	global_load_dwordx4 v[192:195], v201, s[10:11] offset:64
	global_load_dwordx4 v[196:199], v201, s[10:11] offset:96
	v_cmp_lt_i32_e32 vcc, v121, v60
	s_nop 0
	v_mov_b32_e32 v15, v59
	v_cndmask_b32_e64 v12, 32, 0, vcc
	v_add_u32_e32 v16, v12, v121
	v_or_b32_e32 v12, v16, v101
	v_lshlrev_b32_e32 v58, 1, v12
	v_lshrrev_b32_e32 v12, 5, v0
	v_and_b32_e32 v12, 2, v12
	v_bitop3_b32 v14, v102, v100, v12 bitop3:0x36
	v_lshl_add_u64 v[12:13], v[10:11], 0, v[58:59]
	v_lshlrev_b64 v[12:13], 9, v[12:13]
	v_lshlrev_b32_e32 v16, 8, v16
	v_lshl_add_u64 v[12:13], s[4:5], 0, v[12:13]
	v_lshlrev_b32_e32 v14, 4, v14
	v_readfirstlane_b32 s6, v16
	v_add_u32_e32 v17, 0xc000, v16
	v_lshl_add_u64 v[12:13], v[12:13], 0, v[14:15]
	s_mov_b32 m0, s6
	s_mov_b64 s[6:7], 0x100
	v_readfirstlane_b32 s12, v17
	global_load_lds_dwordx4 v[12:13], off
	v_lshl_add_u64 v[12:13], v[12:13], 0, s[6:7]
	s_mov_b32 m0, s12
	v_or_b32_e32 v58, 1, v58
	global_load_lds_dwordx4 v[12:13], off
	v_lshl_add_u64 v[12:13], v[10:11], 0, v[58:59]
	v_lshlrev_b64 v[12:13], 9, v[12:13]
	v_lshl_add_u64 v[12:13], s[4:5], 0, v[12:13]
	v_lshl_add_u64 v[12:13], v[12:13], 0, v[14:15]
	v_add_u32_e32 v14, 0x6000, v16
	v_bfe_u32 v61, v0, 2, 2
	v_readfirstlane_b32 s12, v14
	v_add_u32_e32 v14, 0x12000, v16
	s_mov_b32 m0, s12
	v_readfirstlane_b32 s12, v14
	global_load_lds_dwordx4 v[12:13], off
	v_lshl_add_u64 v[12:13], v[12:13], 0, s[6:7]
	s_mov_b32 m0, s12
	v_add_u32_e32 v18, 0x23800, v117
	global_load_lds_dwordx4 v[12:13], off
	v_or_b32_e32 v12, 4, v121
	v_cmp_lt_i32_e32 vcc, v12, v60
	s_nop 1
	v_cndmask_b32_e64 v13, 32, 0, vcc
	v_add_u32_e32 v16, v13, v12
	v_or_b32_e32 v13, v16, v101
	v_lshlrev_b32_e32 v58, 1, v13
	v_bfe_u32 v12, v12, 2, 2
	v_bitop3_b32 v14, v102, v100, v12 bitop3:0x36
	v_lshl_add_u64 v[12:13], v[10:11], 0, v[58:59]
	v_lshlrev_b64 v[12:13], 9, v[12:13]
	v_lshlrev_b32_e32 v16, 8, v16
	v_lshl_add_u64 v[12:13], s[4:5], 0, v[12:13]
	v_lshlrev_b32_e32 v14, 4, v14
	v_readfirstlane_b32 s12, v16
	v_add_u32_e32 v17, 0xc000, v16
	v_lshl_add_u64 v[12:13], v[12:13], 0, v[14:15]
	s_mov_b32 m0, s12
	v_readfirstlane_b32 s12, v17
	v_or_b32_e32 v58, 1, v58
	global_load_lds_dwordx4 v[12:13], off
	v_lshl_add_u64 v[12:13], v[12:13], 0, s[6:7]
	s_mov_b32 m0, s12
	v_lshl_add_u64 v[10:11], v[10:11], 0, v[58:59]
	global_load_lds_dwordx4 v[12:13], off
	v_lshlrev_b64 v[10:11], 9, v[10:11]
	v_add_u32_e32 v12, 0x6000, v16
	v_lshl_add_u64 v[10:11], s[4:5], 0, v[10:11]
	v_readfirstlane_b32 s4, v12
	v_add_u32_e32 v12, 0x12000, v16
	v_lshl_add_u64 v[10:11], v[10:11], 0, v[14:15]
	s_mov_b32 m0, s4
	v_readfirstlane_b32 s4, v12
	global_load_lds_dwordx4 v[10:11], off
	v_lshl_add_u64 v[10:11], v[10:11], 0, s[6:7]
	s_mov_b32 m0, s4
	s_nop 0
	global_load_lds_dwordx4 v[10:11], off
	s_waitcnt lgkmcnt(0)
	s_barrier
	v_lshlrev_b32_e32 v10, 2, v0
	v_and_b32_e32 v94, 12, v10
	v_or_b32_e32 v120, v94, v61
	v_bitop3_b32 v10, v124, v94, v61 bitop3:0x1e
	v_lshl_or_b32 v14, v10, 4, v18
	v_bitop3_b32 v10, v124, v120, 1 bitop3:0x36
	v_lshl_or_b32 v19, v10, 4, v18
	ds_read_b128 v[10:13], v14
	ds_read_b128 v[62:65], v14 offset:8192
	ds_read_b128 v[14:17], v19
	ds_read_b128 v[66:69], v19 offset:8192
	v_bitop3_b32 v19, v124, v120, 4 bitop3:0x36
	v_lshl_or_b32 v19, v19, 4, v18
	v_bitop3_b32 v20, v124, v120, 5 bitop3:0x36
	v_lshl_or_b32 v20, v20, 4, v18
	ds_read_b128 v[70:73], v19
	ds_read_b128 v[78:81], v19 offset:8192
	ds_read_b128 v[74:77], v20
	ds_read_b128 v[82:85], v20 offset:8192
	v_bitop3_b32 v19, v124, v120, 8 bitop3:0x36
	v_lshl_or_b32 v19, v19, 4, v18
	v_bitop3_b32 v20, v124, v120, 9 bitop3:0x36
	v_lshl_or_b32 v20, v20, 4, v18
	ds_read_b128 v[86:89], v19
	ds_read_b128 v[104:107], v19 offset:8192
	ds_read_b128 v[90:93], v20
	ds_read_b128 v[108:111], v20 offset:8192
	v_bitop3_b32 v19, v124, v120, 12 bitop3:0x36
	v_lshl_or_b32 v19, v19, 4, v18
	v_bitop3_b32 v20, v124, v120, 13 bitop3:0x36
	v_lshl_or_b32 v18, v20, 4, v18
	ds_read_b128 v[126:129], v19
	ds_read_b128 v[134:137], v19 offset:8192
	ds_read_b128 v[130:133], v18
	ds_read_b128 v[138:141], v18 offset:8192
	v_mov_b32_e32 v103, 0x7f
	v_lshlrev_b32_e32 v58, 7, v99
	v_or_b32_e32 v122, 0x18000, v117
	s_waitcnt vmcnt(18) lgkmcnt(0)
	v_mfma_scale_f32_32x32x64_f8f6f4 v[18:33], v[2:9], v[10:17], 0, v103, v103 op_sel_hi:[0,0,0]
	v_lshlrev_b32_e32 v125, 3, v119
	v_or_b32_e32 v123, 0x1a000, v117
	v_mfma_scale_f32_32x32x64_f8f6f4 v[2:17], v[2:9], v[62:69], 0, v103, v103 op_sel_hi:[0,0,0]
	v_and_b32_e32 v62, 12, v95
	s_waitcnt vmcnt(16)
	v_mfma_scale_f32_32x32x64_f8f6f4 v[18:33], v[50:57], v[70:77], v[18:33], v103, v103 op_sel_hi:[0,0,0]
	v_mfma_scale_f32_32x32x64_f8f6f4 v[2:17], v[50:57], v[78:85], v[2:17], v103, v103 op_sel_hi:[0,0,0]
	s_brev_b32 s10, 60
	v_lshlrev_b32_e32 v58, 6, v0
	v_and_b32_e32 v58, 0x4000, v58
	v_or3_b32 v63, v122, v58, v125
	v_or3_b32 v58, v123, v58, v125
	s_waitcnt vmcnt(14)
	v_mfma_scale_f32_32x32x64_f8f6f4 v[18:33], v[42:49], v[86:93], v[18:33], v103, v103 op_sel_hi:[0,0,0]
	v_mfma_scale_f32_32x32x64_f8f6f4 v[2:17], v[42:49], v[104:111], v[2:17], v103, v103 op_sel_hi:[0,0,0]
	s_nop 0
	s_waitcnt vmcnt(12)
	v_mfma_scale_f32_32x32x64_f8f6f4 v[2:17], v[34:41], v[134:141], v[2:17], v103, v103 op_sel_hi:[0,0,0]
	v_mfma_scale_f32_32x32x64_f8f6f4 v[18:33], v[34:41], v[126:133], v[18:33], v103, v103 op_sel_hi:[0,0,0]
	s_waitcnt vmcnt(8)
	s_nop 15
	s_nop 1
	v_fma_f32 v2, v2, s10, v184
	v_fma_f32 v3, v3, s10, v185
	v_fma_f32 v4, v4, s10, v186
	v_fma_f32 v5, v5, s10, v187
	v_cvt_pk_f16_f32 v2, v2, v3
	v_cvt_pk_f16_f32 v3, v4, v5
	v_bitop3_b32 v4, v95, v120, 12 bitop3:0x6c
	v_pk_fma_f32 v[18:19], v[18:19], s[10:11], v[184:185] op_sel_hi:[1,0,1]
	v_pk_fma_f32 v[20:21], v[20:21], s[10:11], v[186:187] op_sel_hi:[1,0,1]
	v_lshlrev_b32_e32 v4, 4, v4
	v_cvt_pk_f16_f32 v18, v18, v19
	v_cvt_pk_f16_f32 v19, v20, v21
	v_or_b32_e32 v5, v63, v4
	v_or_b32_e32 v4, v58, v4
	ds_write_b64 v5, v[18:19]
	ds_write_b64 v4, v[2:3]
	v_pk_fma_f32 v[2:3], v[22:23], s[10:11], v[188:189] op_sel_hi:[1,0,1]
	v_pk_fma_f32 v[4:5], v[6:7], s[10:11], v[188:189] op_sel_hi:[1,0,1]
	v_pk_fma_f32 v[6:7], v[24:25], s[10:11], v[190:191] op_sel_hi:[1,0,1]
	v_cvt_pk_f16_f32 v2, v2, v3
	v_cvt_pk_f16_f32 v3, v6, v7
	v_pk_fma_f32 v[6:7], v[8:9], s[10:11], v[190:191] op_sel_hi:[1,0,1]
	v_cvt_pk_f16_f32 v4, v4, v5
	v_cvt_pk_f16_f32 v5, v6, v7
	v_bitop3_b32 v6, v62, v120, 1 bitop3:0x36
	v_lshlrev_b32_e32 v6, 4, v6
	v_or_b32_e32 v7, v63, v6
	ds_write_b64 v7, v[2:3]
	v_or_b32_e32 v2, v58, v6
	ds_write_b64 v2, v[4:5]
	v_pk_fma_f32 v[2:3], v[26:27], s[10:11], v[192:193] op_sel_hi:[1,0,1]
	v_pk_fma_f32 v[6:7], v[28:29], s[10:11], v[194:195] op_sel_hi:[1,0,1]
	v_cvt_pk_f16_f32 v2, v2, v3
	v_pk_fma_f32 v[4:5], v[10:11], s[10:11], v[192:193] op_sel_hi:[1,0,1]
	v_cvt_pk_f16_f32 v3, v6, v7
	v_pk_fma_f32 v[6:7], v[12:13], s[10:11], v[194:195] op_sel_hi:[1,0,1]
	v_cvt_pk_f16_f32 v4, v4, v5
	v_cvt_pk_f16_f32 v5, v6, v7
	v_bitop3_b32 v6, v62, v120, 2 bitop3:0x36
	v_lshlrev_b32_e32 v6, 4, v6
	v_or_b32_e32 v7, v63, v6
	ds_write_b64 v7, v[2:3]
	v_or_b32_e32 v2, v58, v6
	ds_write_b64 v2, v[4:5]
	v_pk_fma_f32 v[2:3], v[30:31], s[10:11], v[196:197] op_sel_hi:[1,0,1]
	v_pk_fma_f32 v[6:7], v[32:33], s[10:11], v[198:199] op_sel_hi:[1,0,1]
	v_cvt_pk_f16_f32 v2, v2, v3
	v_pk_fma_f32 v[4:5], v[14:15], s[10:11], v[196:197] op_sel_hi:[1,0,1]
	v_cvt_pk_f16_f32 v3, v6, v7
	v_pk_fma_f32 v[6:7], v[16:17], s[10:11], v[198:199] op_sel_hi:[1,0,1]
	v_cvt_pk_f16_f32 v4, v4, v5
	v_cvt_pk_f16_f32 v5, v6, v7
	v_bitop3_b32 v6, v62, v120, 3 bitop3:0x36
	v_lshlrev_b32_e32 v6, 4, v6
	v_or_b32_e32 v7, v63, v6
	ds_write_b64 v7, v[2:3]
	v_or_b32_e32 v2, v58, v6
	ds_write_b64 v2, v[4:5]
	s_waitcnt vmcnt(0) lgkmcnt(0)
	s_barrier
	v_and_b32_e32 v236, 1, v101
	v_lshrrev_b32_e32 v237, 1, v101
	v_xor_b32_e32 v237, v237, v236
	v_lshl_or_b32 v236, v236, 1, v237
	v_lshrrev_b32_e32 v27, 8, v0
	v_lshrrev_b32_e32 v3, 3, v0
	v_and_b32_e32 v3, 16, v3
	v_mul_u32_u24_e32 v28, 0x60, v27
	v_lshlrev_b32_e32 v26, 5, v27
	v_or_b32_e32 v146, v3, v100
	v_or_b32_e32 v147, v28, v100
	v_or_b32_e32 v4, v146, v26
	v_lshlrev_b32_e32 v209, 2, v4
	v_add_u32_e32 v209, 0x27800, v209
	v_lshlrev_b32_e32 v4, 8, v4
	v_or_b32_e32 v5, 0x18000, v4
	v_bitop3_b32 v11, v236, v120, 12 bitop3:0x36
	v_or_b32_e32 v95, 0x1c000, v4
	v_lshlrev_b32_e32 v29, 3, v101
	v_bitop3_b32 v6, v236, v94, v61 bitop3:0x1e
	v_bitop3_b32 v8, v236, v120, 4 bitop3:0x36
	v_bitop3_b32 v10, v236, v120, 8 bitop3:0x36
	v_lshlrev_b32_e32 v94, 4, v11
	v_lshlrev_b32_e32 v6, 4, v6
	v_lshlrev_b32_e32 v8, 4, v8
	v_lshlrev_b32_e32 v58, 4, v10
	v_or_b32_e32 v7, v5, v6
	v_or_b32_e32 v9, v5, v8
	v_or_b32_e32 v10, v5, v58
	v_or_b32_e32 v5, v5, v94
	v_or_b32_e32 v6, v95, v6
	v_or_b32_e32 v60, v95, v8
	ds_read_b128 v[22:25], v7
	ds_read_b128 v[18:21], v9
	ds_read_b128 v[14:17], v10
	ds_read_b128 v[10:13], v5
	ds_read_b128 v[6:9], v6
	ds_read_b128 v[2:5], v60
	v_bfe_u32 v103, v0, 6, 1
	s_movk_i32 s5, 0x2000
	v_mad_u32_u24 v44, v103, 48, v147
	v_lshlrev_b32_e32 v60, 8, v44
	v_lshlrev_b32_e32 v44, 2, v44
	v_or_b32_e32 v35, v95, v58
	v_lshlrev_b32_e32 v58, 14, v99
	v_and_b32_e32 v44, 12, v44
	v_or_b32_e32 v56, v44, v61
	v_bitop3_b32 v44, v236, v44, v61 bitop3:0x1e
	v_lshl_add_u64 v[32:33], s[8:9], 0, v[58:59]
	v_lshlrev_b32_e32 v58, 4, v98
	v_or_b32_e32 v36, v95, v94
	v_lshl_add_u64 v[88:89], v[32:33], 0, v[58:59]
	v_lshl_or_b32 v57, v44, 4, v60
	ds_read_b128 v[40:43], v35
	ds_read_b128 v[106:109], v36
	global_load_dwordx4 v[36:39], v[88:89], off
	global_load_dwordx4 v[32:35], v[88:89], off offset:1024
	ds_read_b128 v[44:47], v57
	v_bitop3_b32 v48, v236, v56, 4 bitop3:0x36
	v_lshl_or_b32 v62, v48, 4, v60
	ds_read_b128 v[48:51], v62
	v_bitop3_b32 v52, v236, v56, 8 bitop3:0x36
	v_lshl_or_b32 v63, v52, 4, v60
	ds_read_b128 v[52:55], v63
	s_waitcnt lgkmcnt(0)
	v_mfma_f32_16x16x32_f16 v[44:47], v[44:47], v[22:25], 0
	v_bitop3_b32 v64, v236, v56, 12 bitop3:0x36
	ds_read_b128 v[56:59], v57 offset:49152
	v_lshl_or_b32 v60, v64, 4, v60
	v_mfma_f32_16x16x32_f16 v[44:47], v[48:51], v[18:21], v[44:47]
	ds_read_b128 v[68:71], v60
	ds_read_b128 v[72:75], v62 offset:49152
	v_mad_u32_u24 v104, v103, 3, 1
	v_lshlrev_b32_e32 v132, 4, v104
	v_mfma_f32_16x16x32_f16 v[44:47], v[52:55], v[14:17], v[44:47]
	v_add_u32_e32 v52, v132, v147
	global_load_dwordx4 v[64:67], v[88:89], off offset:2048
	global_load_dwordx4 v[48:51], v[88:89], off offset:3072
	ds_read_b128 v[76:79], v63 offset:49152
	ds_read_b128 v[80:83], v60 offset:49152
	s_waitcnt lgkmcnt(3)
	v_mfma_f32_16x16x32_f16 v[44:47], v[68:71], v[10:13], v[44:47]
	v_lshlrev_b32_e32 v60, 8, v52
	v_lshlrev_b32_e32 v52, 2, v52
	v_and_b32_e32 v52, 12, v52
	v_mfma_f32_16x16x32_f16 v[44:47], v[56:59], v[6:9], v[44:47]
	v_or_b32_e32 v62, v52, v61
	v_bitop3_b32 v52, v236, v52, v61 bitop3:0x1e
	v_lshl_or_b32 v63, v52, 4, v60
	s_waitcnt lgkmcnt(2)
	v_mfma_f32_16x16x32_f16 v[44:47], v[72:75], v[2:5], v[44:47]
	ds_read_b128 v[52:55], v63
	v_bitop3_b32 v56, v236, v62, 4 bitop3:0x36
	v_lshl_or_b32 v84, v56, 4, v60
	s_waitcnt lgkmcnt(2)
	v_mfma_f32_16x16x32_f16 v[44:47], v[76:79], v[40:43], v[44:47]
	ds_read_b128 v[56:59], v84
	v_bitop3_b32 v68, v236, v62, 8 bitop3:0x36
	v_lshl_or_b32 v85, v68, 4, v60
	s_waitcnt lgkmcnt(2)
	v_mfma_f32_16x16x32_f16 v[110:113], v[80:83], v[106:109], v[44:47]
	ds_read_b128 v[68:71], v63 offset:49152
	v_bitop3_b32 v62, v236, v62, 12 bitop3:0x36
	v_lshl_or_b32 v60, v62, 4, v60
	ds_read_b128 v[44:47], v85
	s_waitcnt lgkmcnt(3)
	v_mfma_f32_16x16x32_f16 v[52:55], v[52:55], v[22:25], 0
	ds_read_b128 v[72:75], v60
	ds_read_b128 v[76:79], v84 offset:49152
	v_mad_u32_u24 v105, v103, 3, 2
	v_lshlrev_b32_e32 v133, 4, v105
	s_waitcnt lgkmcnt(4)
	v_mfma_f32_16x16x32_f16 v[52:55], v[56:59], v[18:21], v[52:55]
	ds_read_b128 v[56:59], v85 offset:49152
	v_add_co_u32_e32 v114, vcc, s15, v88
	s_waitcnt lgkmcnt(3)
	v_mfma_f32_16x16x32_f16 v[44:47], v[44:47], v[14:17], v[52:55]
	v_addc_co_u32_e32 v115, vcc, 0, v89, vcc
	s_waitcnt lgkmcnt(2)
	v_mfma_f32_16x16x32_f16 v[44:47], v[72:75], v[10:13], v[44:47]
	ds_read_b128 v[52:55], v60 offset:49152
	v_add_u32_e32 v60, v133, v147
	v_lshlrev_b32_e32 v72, 8, v60
	v_lshlrev_b32_e32 v60, 2, v60
	v_mfma_f32_16x16x32_f16 v[44:47], v[68:71], v[6:9], v[44:47]
	v_and_b32_e32 v60, 12, v60
	v_or_b32_e32 v68, v60, v61
	v_bitop3_b32 v60, v236, v60, v61 bitop3:0x1e
	v_lshl_or_b32 v69, v60, 4, v72
	s_waitcnt lgkmcnt(2)
	v_mfma_f32_16x16x32_f16 v[44:47], v[76:79], v[2:5], v[44:47]
	ds_read_b128 v[60:63], v69
	v_bitop3_b32 v70, v236, v68, 4 bitop3:0x36
	v_lshl_or_b32 v70, v70, 4, v72
	s_waitcnt lgkmcnt(2)
	v_mfma_f32_16x16x32_f16 v[44:47], v[56:59], v[40:43], v[44:47]
	ds_read_b128 v[56:59], v70
	v_bitop3_b32 v71, v236, v68, 8 bitop3:0x36
	v_lshl_or_b32 v71, v71, 4, v72
	s_waitcnt lgkmcnt(1)
	v_mfma_f32_16x16x32_f16 v[22:25], v[60:63], v[22:25], 0
	v_bitop3_b32 v60, v236, v68, 12 bitop3:0x36
	v_lshl_or_b32 v68, v60, 4, v72
	ds_read_b32 v210, v209
	v_mfma_f32_16x16x32_f16 v[126:129], v[52:55], v[106:109], v[44:47]
	s_nop 2
	ds_read_b128 v[44:47], v71
	ds_read_b128 v[52:55], v69 offset:49152
	ds_read_b128 v[60:63], v70 offset:49152
	s_waitcnt lgkmcnt(4)
	v_mfma_f32_16x16x32_f16 v[18:21], v[56:59], v[18:21], v[22:25]
	ds_read_b128 v[56:59], v71 offset:49152
	s_nop 1
	ds_read_b128 v[22:25], v68
	s_waitcnt lgkmcnt(4)
	v_mfma_f32_16x16x32_f16 v[14:17], v[44:47], v[14:17], v[18:21]
	v_add_co_u32_e32 v44, vcc, s5, v88
	s_movk_i32 s5, 0x3000
	s_nop 0
	ds_read_b128 v[18:21], v68 offset:49152
	s_waitcnt lgkmcnt(1)
	v_mfma_f32_16x16x32_f16 v[10:13], v[22:25], v[10:13], v[14:17]
	v_addc_co_u32_e32 v45, vcc, 0, v89, vcc
	global_load_dwordx4 v[84:87], v[114:115], off offset:1024
	global_load_dwordx4 v[80:83], v[114:115], off offset:2048
	global_load_dwordx4 v[92:95], v[44:45], off offset:-4096
	global_load_dwordx4 v[76:79], v[44:45], off
	v_mfma_f32_16x16x32_f16 v[6:9], v[52:55], v[6:9], v[10:13]
	global_load_dwordx4 v[72:75], v[44:45], off offset:1024
	global_load_dwordx4 v[68:71], v[44:45], off offset:2048
	global_load_dwordx4 v[52:55], v[44:45], off offset:3072
	v_mov_b32_e32 v13, 0xff61b1e6
	v_mfma_f32_16x16x32_f16 v[2:5], v[60:63], v[2:5], v[6:9]
	s_nop 2
	v_add_co_u32_e32 v6, vcc, s5, v88
	v_mfma_f32_16x16x32_f16 v[2:5], v[56:59], v[40:43], v[2:5]
	s_nop 0
	v_addc_co_u32_e32 v7, vcc, 0, v89, vcc
	global_load_dwordx4 v[88:91], v[114:115], off offset:3072
	global_load_dwordx4 v[60:63], v[6:7], off
	global_load_dwordx4 v[56:59], v[6:7], off offset:1024
	global_load_dwordx4 v[44:47], v[6:7], off offset:2048
	global_load_dwordx4 v[40:43], v[6:7], off offset:3072
	s_waitcnt lgkmcnt(0)
	v_mfma_f32_16x16x32_f16 v[16:19], v[18:21], v[106:109], v[2:5]
	s_mov_b32 s5, 0xff61b1e6
	s_nop 0
	v_or_b32_e32 v3, s14, v146
	v_mov_b32_e32 v4, 0x7df
	v_med3_u32 v3, v3, 32, v4
	v_or_b32_e32 v4, v97, v102
	v_sub_u32_e32 v3, v4, v3
	v_add_f32_e32 v2, s32, v210
	v_add_u32_e32 v3, 32, v3
	v_mad_u32_u24 v4, v103, 48, v3
	s_movk_i32 s4, 0x41
	v_add_f32_e32 v5, v2, v110
	v_mul_f32_e32 v5, 0x3db8aa3b, v5
	v_cmp_gt_u32_e32 vcc, s4, v4
	v_add_u32_e32 v6, 1, v4
	v_add_f32_e32 v7, v2, v111
	v_cndmask_b32_e32 v5, v13, v5, vcc
	v_mul_f32_e32 v7, 0x3db8aa3b, v7
	v_cmp_gt_u32_e32 vcc, s4, v6
	v_add_u32_e32 v8, 2, v4
	v_add_f32_e32 v9, v2, v112
	v_cndmask_b32_e32 v6, v13, v7, vcc
	v_mul_f32_e32 v9, 0x3db8aa3b, v9
	v_cmp_gt_u32_e32 vcc, s4, v8
	v_add_u32_e32 v4, 3, v4
	v_max3_f32 v7, v5, s5, v6
	v_cndmask_b32_e32 v8, v13, v9, vcc
	v_add_f32_e32 v9, v2, v113
	v_mul_f32_e32 v9, 0x3db8aa3b, v9
	v_cmp_gt_u32_e32 vcc, s4, v4
	v_add_u32_e32 v11, v3, v132
	v_add_f32_e32 v12, v2, v127
	v_cndmask_b32_e32 v10, v13, v9, vcc
	v_max3_f32 v4, v7, v8, v10
	v_add_f32_e32 v7, v2, v126
	v_mul_f32_e32 v7, 0x3db8aa3b, v7
	v_cmp_gt_u32_e32 vcc, s4, v11
	v_add_u32_e32 v9, 1, v11
	v_mul_f32_e32 v12, 0x3db8aa3b, v12
	v_cndmask_b32_e32 v7, v13, v7, vcc
	v_cmp_gt_u32_e32 vcc, s4, v9
	v_add_f32_e32 v14, v2, v128
	v_mul_f32_e32 v14, 0x3db8aa3b, v14
	v_cndmask_b32_e32 v9, v13, v12, vcc
	v_add_u32_e32 v12, 2, v11
	v_cmp_gt_u32_e32 vcc, s4, v12
	v_add_u32_e32 v11, 3, v11
	v_add_u32_e32 v3, v3, v133
	v_cndmask_b32_e32 v12, v13, v14, vcc
	v_add_f32_e32 v14, v2, v129
	v_mul_f32_e32 v14, 0x3db8aa3b, v14
	v_cmp_gt_u32_e32 vcc, s4, v11
	v_add_f32_e32 v11, v2, v16
	v_mul_f32_e32 v11, 0x3db8aa3b, v11
	v_cndmask_b32_e32 v15, v13, v14, vcc
	v_cmp_gt_u32_e32 vcc, s4, v3
	v_add_u32_e32 v14, 1, v3
	v_add_f32_e32 v16, v2, v17
	v_cndmask_b32_e32 v11, v13, v11, vcc
	v_mul_f32_e32 v16, 0x3db8aa3b, v16
	v_cmp_gt_u32_e32 vcc, s4, v14
	v_add_f32_e32 v17, v2, v18
	v_max3_f32 v4, v4, v7, v9
	v_cndmask_b32_e32 v14, v13, v16, vcc
	v_add_u32_e32 v16, 2, v3
	v_mul_f32_e32 v17, 0x3db8aa3b, v17
	v_cmp_gt_u32_e32 vcc, s4, v16
	v_add_u32_e32 v3, 3, v3
	v_add_f32_e32 v2, v2, v19
	v_max3_f32 v4, v4, v12, v15
	v_cndmask_b32_e32 v16, v13, v17, vcc
	v_mul_f32_e32 v2, 0x3db8aa3b, v2
	v_cmp_gt_u32_e32 vcc, s4, v3
	v_max3_f32 v4, v4, v11, v14
	v_lshlrev_b32_e32 v126, 5, v99
	v_cndmask_b32_e32 v17, v13, v2, vcc
	v_max3_f32 v2, v4, v16, v17
	v_mov_b32_e32 v3, v2
	v_lshlrev_b32_e32 v127, 2, v119
	v_lshrrev_b32_e32 v4, 7, v0
	v_cmp_gt_u32_e32 vcc, 16, v98
	v_permlane16_swap_b32_e32 v3, v2
	v_max_f32_e32 v2, v2, v3
	v_mov_b32_e32 v3, v2
	s_nop 1
	v_permlane32_swap_b32_e32 v3, v2
	v_max_f32_e32 v13, v2, v3
	v_and_b32_e32 v2, 0x180, v0
	v_or_b32_e32 v2, 0x23400, v2
	v_lshlrev_b32_e32 v3, 2, v100
	s_and_saveexec_b64 s[4:5], vcc
	v_lshlrev_b32_e32 v18, 6, v103
	v_add3_u32 v18, v2, v18, v3
	ds_write_b32 v18, v13
	s_or_b64 exec, exec, s[4:5]
	v_lshlrev_b32_e32 v18, 4, v103
	v_bitop3_b32 v19, v18, 16, v100 bitop3:0x36
	v_lshl_add_u32 v2, v19, 2, v2
	s_waitcnt lgkmcnt(0)
	s_barrier
	ds_read_b32 v19, v2
	v_max_f32_e32 v13, v13, v13
	v_mul_u32_u24_e32 v20, 0xd00, v4
	v_or_b32_e32 v2, 1, v124
	s_waitcnt lgkmcnt(0)
	v_max_f32_e32 v19, v19, v19
	v_max_f32_e32 v19, v13, v19
	v_sub_f32_e32 v5, v5, v19
	v_exp_f32_e32 v5, v5
	v_sub_f32_e32 v6, v6, v19
	v_exp_f32_e32 v6, v6
	v_sub_f32_e32 v8, v8, v19
	v_mul_u32_u24_e32 v13, 0xd0, v100
	v_exp_f32_e32 v8, v8
	v_sub_f32_e32 v10, v10, v19
	v_add3_u32 v20, v13, v20, v29
	v_exp_f32_e32 v10, v10
	v_or_b32_e32 v22, 0x20000, v20
	v_add_f32_e32 v20, 0, v5
	v_add_f32_e32 v20, v20, v6
	v_add_f32_e32 v20, v20, v8
	v_add_f32_e32 v23, v20, v10
	v_cvt_pk_f16_f32 v21, v8, v10
	v_cvt_pk_f16_f32 v20, v5, v6
	v_mad_u32_u24 v5, v103, s16, v22
	ds_write_b64 v5, v[20:21]
	v_sub_f32_e32 v5, v7, v19
	v_exp_f32_e32 v5, v5
	v_sub_f32_e32 v6, v9, v19
	v_exp_f32_e32 v6, v6
	v_sub_f32_e32 v7, v12, v19
	v_exp_f32_e32 v7, v7
	v_sub_f32_e32 v8, v15, v19
	v_exp_f32_e32 v8, v8
	v_sub_f32_e32 v10, v11, v19
	v_add_f32_e32 v9, v23, v5
	v_exp_f32_e32 v10, v10
	v_sub_f32_e32 v11, v14, v19
	v_add_f32_e32 v9, v9, v6
	v_exp_f32_e32 v11, v11
	v_sub_f32_e32 v12, v16, v19
	v_add_f32_e32 v9, v9, v7
	v_exp_f32_e32 v12, v12
	v_sub_f32_e32 v14, v17, v19
	v_add_f32_e32 v9, v9, v8
	v_exp_f32_e32 v14, v14
	v_add_f32_e32 v9, v9, v10
	v_add_f32_e32 v9, v9, v11
	v_add_f32_e32 v9, v9, v12
	v_add_f32_e32 v9, v9, v14
	v_mov_b32_e32 v15, v9
	v_cvt_pk_f16_f32 v7, v7, v8
	v_cvt_pk_f16_f32 v6, v5, v6
	v_lshl_add_u32 v5, v104, 5, v22
	ds_write_b64 v5, v[6:7]
	v_permlane16_swap_b32_e32 v15, v9
	v_add_f32_e32 v5, v9, v15
	v_mov_b32_e32 v6, v5
	s_movk_i32 s7, 0xd00
	s_mov_b32 s6, 0x20000
	v_cvt_pk_f16_f32 v9, v12, v14
	v_cvt_pk_f16_f32 v8, v10, v11
	v_lshl_add_u32 v7, v105, 5, v22
	ds_write_b64 v7, v[8:9]
	v_permlane32_swap_b32_e32 v6, v5
	s_and_saveexec_b64 s[4:5], vcc
	s_cbranch_execz .LBB1_4
	v_lshlrev_b32_e32 v4, 5, v4
	v_or_b32_e32 v7, v18, v100
	v_lshlrev_b32_e32 v4, 2, v4
	v_lshlrev_b32_e32 v7, 2, v7
	s_mov_b32 s8, 0x23600
	v_add3_u32 v4, v7, v4, s8
	v_add_f32_e32 v5, v5, v6
	ds_write_b32 v4, v5
